# speedup vs baseline: 1.1371x; 1.0408x over previous
.Lco_noin1:
	s_lshl_b32 s11, s75, 6
	v_add_u32_e32 v69, s11, v73
	s_and_b32 s12, s10, 3
	s_lshl_b32 s12, s12, 4
	v_lshrrev_b32_e32 v0, 2, v73
	v_add_u32_e32 v0, s12, v0
	v_and_b32_e32 v1, 3, v73
	v_mul_u32_u24_e32 v49, 0x50, v0
	v_lshl_add_u32 v49, v1, 4, v49
	v_add_u32_e32 v0, s11, v0
	v_lshlrev_b32_e32 v1, 2, v1
	v_add_u32_e32 v1, s3, v1
	v_lshl_add_u32 v0, v0, 9, v1
	v_lshlrev_b32_e32 v0, 2, v0
	s_cmp_gt_u32 s10, 3
	s_cselect_b64 s[16:17], s[62:63], s[46:47]
	s_cselect_b64 s[18:19], s[52:53], s[62:63]
	s_cselect_b64 s[20:21], s[54:55], s[62:63]
	s_cselect_b32 s13, 0x200000, 0
	s_cselect_b32 s14, 0, 0x100000
	s_cselect_b32 s15, 0x3c00, 0
	v_add_u32_e32 v1, s13, v0
	v_add_u32_e32 v2, s14, v0
	v_add_u32_e32 v49, s15, v49
	v_lshlrev_b32_e32 v3, 2, v69
	global_load_dwordx4 v[36:39], v1, s[16:17]
	global_load_dwordx4 v[40:43], v0, s[18:19]
	global_load_dwordx4 v[44:47], v2, s[20:21]
	global_load_dword v48, v3, s[60:61]
	v_cmp_gt_u32_e32 vcc, 4, v98
	s_and_saveexec_b64 s[14:15], vcc
	v_mov_b32_e32 v4, 0x26c10
	v_lshl_add_u32 v4, v98, 2, v4
	ds_write_b32 v4, v34
	s_mov_b64 exec, s[14:15]
	v_cmp_eq_u32_e32 vcc, 0, v98
	s_and_saveexec_b64 s[14:15], vcc
	v_mov_b32_e32 v4, 0x26c00
	ds_write2_b32 v4, v34, v34 offset1:1
	s_mov_b64 exec, s[14:15]
	v_mov_b32_e32 v159, 0
	v_mov_b32_e32 v9, 0
	v_mov_b32_e32 v18, 0
	v_mov_b32_e32 v129, 0
	v_mov_b32_e32 v130, 0
	v_mov_b32_e32 v71, 0
	v_mov_b32_e32 v158, 0
	v_mov_b32_e32 v131, 0
	v_mov_b32_e32 v19, 0
	v_mov_b32_e32 v132, 0
	v_mov_b32_e32 v133, 0
	v_mov_b32_e32 v81, 0
	v_mov_b32_e32 v157, 0
	v_mov_b32_e32 v134, 0
	v_mov_b32_e32 v20, 0
	v_mov_b32_e32 v135, 0
	v_mov_b32_e32 v136, 0
	v_mov_b32_e32 v85, 0
	v_mov_b32_e32 v156, 0
	v_mov_b32_e32 v137, 0
	v_mov_b32_e32 v21, 0
	v_mov_b32_e32 v138, 0
	v_mov_b32_e32 v139, 0
	v_mov_b32_e32 v86, 0
	v_mov_b32_e32 v155, 0
	v_mov_b32_e32 v140, 0
	v_mov_b32_e32 v22, 0
	v_mov_b32_e32 v141, 0
	v_mov_b32_e32 v142, 0
	v_mov_b32_e32 v87, 0
	v_mov_b32_e32 v154, 0
	v_mov_b32_e32 v143, 0
	v_mov_b32_e32 v23, 0
	v_mov_b32_e32 v144, 0
	v_mov_b32_e32 v145, 0
	v_mov_b32_e32 v88, 0
	v_mov_b32_e32 v153, 0
	v_mov_b32_e32 v146, 0
	v_mov_b32_e32 v24, 0
	v_mov_b32_e32 v147, 0
	v_mov_b32_e32 v148, 0
	v_mov_b32_e32 v89, 0
	v_mov_b32_e32 v149, 0
	v_mov_b32_e32 v150, 0
	v_mov_b32_e32 v25, 0
	v_mov_b32_e32 v151, 0
	v_mov_b32_e32 v152, 0
	v_mov_b32_e32 v90, 0
	v_mov_b32_e32 v128, 0
	v_mov_b32_e32 v121, 0
	v_mov_b32_e32 v26, 0
	v_mov_b32_e32 v123, 0
	v_mov_b32_e32 v125, 0
	v_mov_b32_e32 v91, 0
	v_mov_b32_e32 v127, 0
	v_mov_b32_e32 v122, 0
	v_mov_b32_e32 v27, 0
	v_mov_b32_e32 v124, 0
	v_mov_b32_e32 v126, 0
	v_mov_b32_e32 v92, 0
	v_mov_b32_e32 v120, 0
	v_mov_b32_e32 v112, 0
	v_mov_b32_e32 v28, 0
	v_mov_b32_e32 v115, 0
	v_mov_b32_e32 v117, 0
	v_mov_b32_e32 v93, 0
	v_mov_b32_e32 v119, 0
	v_mov_b32_e32 v113, 0
	v_mov_b32_e32 v29, 0
	v_mov_b32_e32 v116, 0
	v_mov_b32_e32 v118, 0
	v_mov_b32_e32 v94, 0
	v_mov_b32_e32 v114, 0
	v_mov_b32_e32 v100, 0
	v_mov_b32_e32 v30, 0
	v_mov_b32_e32 v103, 0
	v_mov_b32_e32 v107, 0
	v_mov_b32_e32 v95, 0
	v_mov_b32_e32 v111, 0
	v_mov_b32_e32 v101, 0
	v_mov_b32_e32 v31, 0
	v_mov_b32_e32 v104, 0
	v_mov_b32_e32 v108, 0
	v_mov_b32_e32 v96, 0
	v_mov_b32_e32 v17, 0
	v_mov_b32_e32 v102, 0
	v_mov_b32_e32 v32, 0
	v_mov_b32_e32 v105, 0
	v_mov_b32_e32 v109, 0
	v_mov_b32_e32 v97, 0
	v_mov_b32_e32 v8, 0
	v_mov_b32_e32 v16, 0
	v_mov_b32_e32 v33, 0
	v_mov_b32_e32 v106, 0
	v_mov_b32_e32 v110, 0
	v_mov_b32_e32 v99, 0
	s_waitcnt vmcnt(0)
	ds_write_b128 v49, v[36:39]
	ds_write_b128 v49, v[40:43] offset:5120
	ds_write_b128 v49, v[44:47] offset:10240
	v_mul_u32_u24_e32 v0, 0x50, v73
	s_lshl_b32 s12, s10, 3
	v_add_u32_e32 v0, s12, v0
	s_lshl_b32 s12, s10, 1
	s_add_i32 s13, s3, s12
	s_waitcnt lgkmcnt(0)
	s_barrier
	ds_read_b64 v[36:37], v0
	ds_read_b64 v[38:39], v0 offset:5120
	ds_read_b64 v[40:41], v0 offset:10240
	ds_read_b64 v[42:43], v0 offset:15360
	ds_read_b64 v[44:45], v0 offset:20480
	ds_read_b64 v[46:47], v0 offset:25600
	s_movk_i32 s84, 0x1000
	s_mov_b64 s[34:35], 0
	s_waitcnt lgkmcnt(0)
	v_mul_f32_e64 v50, v48, |v36|
	v_cmp_neq_f32_e64 s[16:17], 0, v38
	v_cmp_neq_f32_e64 s[18:19], 0, v40
	v_cmp_neq_f32_e64 s[20:21], 0, v42
	v_cmp_neq_f32_e64 s[22:23], 0, v50
	v_cndmask_b32_e64 v51, v42, v40, s[18:19]
	v_cndmask_b32_e64 v52, 2, 1, s[18:19]
	v_cndmask_b32_e64 v51, v51, v38, s[16:17]
	v_cndmask_b32_e64 v52, v52, 0, s[16:17]
	s_or_b64 s[24:25], s[16:17], s[18:19]
	s_and_b64 s[28:29], s[16:17], s[18:19]
	s_and_b64 s[30:31], s[24:25], s[20:21]
	s_or_b64 s[24:25], s[24:25], s[20:21]
	s_or_b64 s[28:29], s[28:29], s[30:31]
	s_and_b64 s[26:27], s[22:23], s[24:25]
	s_and_b64 s[28:29], s[28:29], s[22:23]
	s_or_b64 s[34:35], s[34:35], s[28:29]
	v_lshlrev_b32_e64 v53, v52, s84
	v_lshlrev_b32_e32 v54, 3, v69
	v_sub_u32_e32 v54, v54, v53
	v_and_b32_e32 v56, 0xffff, v54
	v_mul_f32_e32 v57, v50, v51
	v_mul_f32_e32 v58, v44, v51
	v_mul_f32_e32 v59, v46, v51
	v_and_b32_e32 v55, 0x7fffffff, v50
	v_div_scale_f32 v61, s[30:31], v55, v55, 2.0
	v_rcp_f32_e32 v62, v61
	v_div_scale_f32 v55, vcc, 2.0, v55, 2.0
	v_fma_f32 v53, -v61, v62, 1.0
	v_fmac_f32_e32 v62, v53, v62
	v_mul_f32_e32 v53, v55, v62
	v_fma_f32 v54, -v61, v53, v55
	v_fmac_f32_e32 v53, v54, v62
	v_fma_f32 v55, -v61, v53, v55
	v_div_fmas_f32 v55, v55, v62, v53
	v_div_fixup_f32 v60, v55, |v50|, 2.0
	v_mbcnt_lo_u32_b32 v53, s26, 0
	v_mbcnt_hi_u32_b32 v53, s27, v53
	s_bcnt1_i32_b64 s85, s[26:27]
	s_add_i32 s36, s13, 0
	s_lshl_b32 s36, s36, 3
	s_add_i32 s87, s36, s75
	s_lshl_b32 s37, s87, 11
	s_add_i32 s37, s37, 0x800000
	v_lshl_add_u32 v4, v53, 5, s37
	s_and_saveexec_b64 s[38:39], s[26:27]
	s_cbranch_execz .Lco_nost0
	global_store_dwordx4 v4, v[56:59], s[66:67] sc1
	global_store_dword v4, v60, s[66:67] offset:16 sc1
